# dn epilogue: the eight per-row-group gate loads hoisted to one prefetch (no per-group vmcnt(0)), plus XCD-aware dn deal
# baseline (speedup 1.0000x reference)
.LBB0_1377:
	s_lshl_b32 s4, s7, 8
	v_add_u32_e32 v6, s4, v1
	v_cmp_gt_i32_e32 vcc, s63, v6
	s_mul_i32 s7, s14, 0x500
	v_lshl_or_b32 v4, s6, 8, v228
	v_readlane_b32 s34, v254, 59
	v_readlane_b32 s35, v254, 60
	s_nop 1
	v_add_u32_e32 v60, s4, v1
	v_add_u32_e32 v60, s7, v60
	v_ashrrev_i32_e32 v61, 31, v60
	v_lshl_add_u64 v[60:61], v[60:61], 2, s[34:35]
	global_load_dword v52, v[60:61], off offset:0
	global_load_dword v53, v[60:61], off offset:64
	global_load_dword v54, v[60:61], off offset:128
	global_load_dword v55, v[60:61], off offset:192
	global_load_dword v56, v[60:61], off offset:512
	global_load_dword v57, v[60:61], off offset:576
	global_load_dword v58, v[60:61], off offset:640
	global_load_dword v59, v[60:61], off offset:704
	s_waitcnt vmcnt(0)
	s_and_saveexec_b64 s[16:17], vcc
	v_readlane_b32 s34, v254, 59
	v_readlane_b32 s35, v254, 60
	s_cbranch_execz .LBB0_1379
	v_ashrrev_i32_e32 v7, 31, v6
	v_ashrrev_i32_e32 v5, 31, v4
	v_mul_f32_e32 v2, 0x3b800000, v52
	v_pk_mul_f32 v[10:11], v[194:195], v[2:3] op_sel_hi:[1,0]
	v_pk_mul_f32 v[8:9], v[192:193], v[2:3] op_sel_hi:[1,0]
	v_pk_mul_f32 v[12:13], v[190:191], v[2:3] op_sel_hi:[1,0]
	v_cvt_pk_bf16_f32 v8, v8, v9
	v_cvt_pk_bf16_f32 v9, v10, v11
	v_cvt_pk_bf16_f32 v11, v12, v13
	v_mad_i64_i32 v[12:13], s[28:29], s14, v239, v[6:7]
	v_lshlrev_b64 v[12:13], 12, v[12:13]
	v_pk_mul_f32 v[14:15], v[188:189], v[2:3] op_sel_hi:[1,0]
	v_lshl_add_u64 v[12:13], s[70:71], 0, v[12:13]
	v_cvt_pk_bf16_f32 v10, v14, v15
	v_lshl_add_u64 v[12:13], v[4:5], 1, v[12:13]
	global_store_dwordx4 v[12:13], v[8:11], off
	v_pk_mul_f32 v[14:15], v[182:183], v[2:3] op_sel_hi:[1,0]
	v_pk_mul_f32 v[16:17], v[180:181], v[2:3] op_sel_hi:[1,0]
	v_pk_mul_f32 v[10:11], v[186:187], v[2:3] op_sel_hi:[1,0]
	v_pk_mul_f32 v[8:9], v[184:185], v[2:3] op_sel_hi:[1,0]
	s_nop 0
	v_cvt_pk_bf16_f32 v8, v8, v9
	v_cvt_pk_bf16_f32 v9, v10, v11
	v_cvt_pk_bf16_f32 v10, v16, v17
	v_cvt_pk_bf16_f32 v11, v14, v15
	global_store_dwordx4 v[12:13], v[8:11], off offset:256
.LBB0_1379:
	s_or_b64 exec, exec, s[16:17]
	s_nop 0
	v_add_u32_e32 v8, s4, v241
	v_cmp_gt_i32_e32 vcc, s63, v8
	s_and_saveexec_b64 s[16:17], vcc
	s_cbranch_execz .LBB0_1381
	v_ashrrev_i32_e32 v9, 31, v8
	v_mad_i64_i32 v[8:9], s[28:29], s14, v239, v[8:9]
	v_lshlrev_b64 v[8:9], 12, v[8:9]
	v_lshl_add_u64 v[8:9], s[70:71], 0, v[8:9]
	v_ashrrev_i32_e32 v5, 31, v4
	v_mul_f32_e32 v2, 0x3b800000, v53
	v_pk_mul_f32 v[12:13], v[178:179], v[2:3] op_sel_hi:[1,0]
	v_pk_mul_f32 v[10:11], v[176:177], v[2:3] op_sel_hi:[1,0]
	v_pk_mul_f32 v[14:15], v[174:175], v[2:3] op_sel_hi:[1,0]
	v_pk_mul_f32 v[16:17], v[172:173], v[2:3] op_sel_hi:[1,0]
	v_cvt_pk_bf16_f32 v10, v10, v11
	v_cvt_pk_bf16_f32 v11, v12, v13
	v_cvt_pk_bf16_f32 v12, v16, v17
	v_cvt_pk_bf16_f32 v13, v14, v15
	v_lshl_add_u64 v[14:15], v[4:5], 1, v[8:9]
	global_store_dwordx4 v[14:15], v[10:13], off
	v_pk_mul_f32 v[8:9], v[168:169], v[2:3] op_sel_hi:[1,0]
	v_pk_mul_f32 v[16:17], v[164:165], v[2:3] op_sel_hi:[1,0]
	v_pk_mul_f32 v[10:11], v[170:171], v[2:3] op_sel_hi:[1,0]
	v_pk_mul_f32 v[12:13], v[166:167], v[2:3] op_sel_hi:[1,0]
	v_cvt_pk_bf16_f32 v8, v8, v9
	v_cvt_pk_bf16_f32 v9, v10, v11
	v_cvt_pk_bf16_f32 v10, v16, v17
	v_cvt_pk_bf16_f32 v11, v12, v13
	global_store_dwordx4 v[14:15], v[8:11], off offset:256
.LBB0_1381:
	s_or_b64 exec, exec, s[16:17]
	s_nop 0
	v_add_u32_e32 v8, s4, v242
	v_cmp_gt_i32_e32 vcc, s63, v8
	s_and_saveexec_b64 s[16:17], vcc
	s_cbranch_execz .LBB0_1383
	v_ashrrev_i32_e32 v9, 31, v8
	v_mad_i64_i32 v[8:9], s[28:29], s14, v239, v[8:9]
	v_lshlrev_b64 v[8:9], 12, v[8:9]
	v_lshl_add_u64 v[8:9], s[70:71], 0, v[8:9]
	v_ashrrev_i32_e32 v5, 31, v4
	v_mul_f32_e32 v2, 0x3b800000, v54
	v_pk_mul_f32 v[12:13], v[162:163], v[2:3] op_sel_hi:[1,0]
	v_pk_mul_f32 v[10:11], v[160:161], v[2:3] op_sel_hi:[1,0]
	v_pk_mul_f32 v[14:15], v[158:159], v[2:3] op_sel_hi:[1,0]
	v_pk_mul_f32 v[16:17], v[156:157], v[2:3] op_sel_hi:[1,0]
	v_cvt_pk_bf16_f32 v10, v10, v11
	v_cvt_pk_bf16_f32 v11, v12, v13
	v_cvt_pk_bf16_f32 v12, v16, v17
	v_cvt_pk_bf16_f32 v13, v14, v15
	v_lshl_add_u64 v[14:15], v[4:5], 1, v[8:9]
	global_store_dwordx4 v[14:15], v[10:13], off
	v_pk_mul_f32 v[8:9], v[152:153], v[2:3] op_sel_hi:[1,0]
	v_pk_mul_f32 v[16:17], v[148:149], v[2:3] op_sel_hi:[1,0]
	v_pk_mul_f32 v[10:11], v[154:155], v[2:3] op_sel_hi:[1,0]
	v_pk_mul_f32 v[12:13], v[150:151], v[2:3] op_sel_hi:[1,0]
	v_cvt_pk_bf16_f32 v8, v8, v9
	v_cvt_pk_bf16_f32 v9, v10, v11
	v_cvt_pk_bf16_f32 v10, v16, v17
	v_cvt_pk_bf16_f32 v11, v12, v13
	global_store_dwordx4 v[14:15], v[8:11], off offset:256
.LBB0_1383:
	s_or_b64 exec, exec, s[16:17]
	s_nop 0
	v_add_u32_e32 v8, s4, v243
	v_cmp_gt_i32_e32 vcc, s63, v8
	s_and_saveexec_b64 s[16:17], vcc
	s_cbranch_execz .LBB0_1385
	v_ashrrev_i32_e32 v9, 31, v8
	v_mad_i64_i32 v[8:9], s[4:5], s14, v239, v[8:9]
	v_lshlrev_b64 v[8:9], 12, v[8:9]
	v_lshl_add_u64 v[8:9], s[70:71], 0, v[8:9]
	v_ashrrev_i32_e32 v5, 31, v4
	v_mul_f32_e32 v2, 0x3b800000, v55
	v_pk_mul_f32 v[12:13], v[146:147], v[2:3] op_sel_hi:[1,0]
	v_pk_mul_f32 v[10:11], v[144:145], v[2:3] op_sel_hi:[1,0]
	v_pk_mul_f32 v[14:15], v[142:143], v[2:3] op_sel_hi:[1,0]
	v_pk_mul_f32 v[16:17], v[140:141], v[2:3] op_sel_hi:[1,0]
	v_cvt_pk_bf16_f32 v10, v10, v11
	v_cvt_pk_bf16_f32 v11, v12, v13
	v_cvt_pk_bf16_f32 v12, v16, v17
	v_cvt_pk_bf16_f32 v13, v14, v15
	v_lshl_add_u64 v[14:15], v[4:5], 1, v[8:9]
	global_store_dwordx4 v[14:15], v[10:13], off
	v_pk_mul_f32 v[8:9], v[136:137], v[2:3] op_sel_hi:[1,0]
	v_pk_mul_f32 v[16:17], v[132:133], v[2:3] op_sel_hi:[1,0]
	v_pk_mul_f32 v[10:11], v[138:139], v[2:3] op_sel_hi:[1,0]
	v_pk_mul_f32 v[12:13], v[134:135], v[2:3] op_sel_hi:[1,0]
	v_cvt_pk_bf16_f32 v8, v8, v9
	v_cvt_pk_bf16_f32 v9, v10, v11
	v_cvt_pk_bf16_f32 v10, v16, v17
	v_cvt_pk_bf16_f32 v11, v12, v13
	global_store_dwordx4 v[14:15], v[8:11], off offset:256
.LBB0_1385:
	s_or_b64 exec, exec, s[16:17]
	s_nop 0
	v_add_u32_e32 v8, 0x80, v6
	v_cmp_gt_i32_e32 vcc, s63, v8
	s_and_saveexec_b64 s[16:17], vcc
	s_cbranch_execz .LBB0_1387
	v_ashrrev_i32_e32 v9, 31, v8
	v_mad_i64_i32 v[8:9], s[4:5], s14, v239, v[8:9]
	v_lshlrev_b64 v[8:9], 12, v[8:9]
	v_lshl_add_u64 v[8:9], s[70:71], 0, v[8:9]
	v_ashrrev_i32_e32 v5, 31, v4
	v_mul_f32_e32 v2, 0x3b800000, v56
	v_pk_mul_f32 v[12:13], v[130:131], v[2:3] op_sel_hi:[1,0]
	v_pk_mul_f32 v[10:11], v[128:129], v[2:3] op_sel_hi:[1,0]
	v_pk_mul_f32 v[14:15], v[126:127], v[2:3] op_sel_hi:[1,0]
	v_pk_mul_f32 v[16:17], v[124:125], v[2:3] op_sel_hi:[1,0]
	v_cvt_pk_bf16_f32 v10, v10, v11
	v_cvt_pk_bf16_f32 v11, v12, v13
	v_cvt_pk_bf16_f32 v12, v16, v17
	v_cvt_pk_bf16_f32 v13, v14, v15
	v_lshl_add_u64 v[14:15], v[4:5], 1, v[8:9]
	global_store_dwordx4 v[14:15], v[10:13], off
	v_pk_mul_f32 v[8:9], v[120:121], v[2:3] op_sel_hi:[1,0]
	v_pk_mul_f32 v[16:17], v[116:117], v[2:3] op_sel_hi:[1,0]
	v_pk_mul_f32 v[10:11], v[122:123], v[2:3] op_sel_hi:[1,0]
	v_pk_mul_f32 v[12:13], v[118:119], v[2:3] op_sel_hi:[1,0]
	v_cvt_pk_bf16_f32 v8, v8, v9
	v_cvt_pk_bf16_f32 v9, v10, v11
	v_cvt_pk_bf16_f32 v10, v16, v17
	v_cvt_pk_bf16_f32 v11, v12, v13
	global_store_dwordx4 v[14:15], v[8:11], off offset:256
.LBB0_1387:
	s_or_b64 exec, exec, s[16:17]
	s_nop 0
	v_add_u32_e32 v8, 0x90, v6
	v_cmp_gt_i32_e32 vcc, s63, v8
	s_and_saveexec_b64 s[16:17], vcc
	s_cbranch_execz .LBB0_1389
	v_ashrrev_i32_e32 v9, 31, v8
	v_mad_i64_i32 v[8:9], s[4:5], s14, v239, v[8:9]
	v_lshlrev_b64 v[8:9], 12, v[8:9]
	v_lshl_add_u64 v[8:9], s[70:71], 0, v[8:9]
	v_ashrrev_i32_e32 v5, 31, v4
	v_mul_f32_e32 v2, 0x3b800000, v57
	v_pk_mul_f32 v[12:13], v[114:115], v[2:3] op_sel_hi:[1,0]
	v_pk_mul_f32 v[10:11], v[112:113], v[2:3] op_sel_hi:[1,0]
	v_pk_mul_f32 v[14:15], v[110:111], v[2:3] op_sel_hi:[1,0]
	v_pk_mul_f32 v[16:17], v[108:109], v[2:3] op_sel_hi:[1,0]
	v_cvt_pk_bf16_f32 v10, v10, v11
	v_cvt_pk_bf16_f32 v11, v12, v13
	v_cvt_pk_bf16_f32 v12, v16, v17
	v_cvt_pk_bf16_f32 v13, v14, v15
	v_lshl_add_u64 v[14:15], v[4:5], 1, v[8:9]
	global_store_dwordx4 v[14:15], v[10:13], off
	v_pk_mul_f32 v[8:9], v[104:105], v[2:3] op_sel_hi:[1,0]
	v_pk_mul_f32 v[16:17], v[100:101], v[2:3] op_sel_hi:[1,0]
	v_pk_mul_f32 v[10:11], v[106:107], v[2:3] op_sel_hi:[1,0]
	v_pk_mul_f32 v[12:13], v[102:103], v[2:3] op_sel_hi:[1,0]
	v_cvt_pk_bf16_f32 v8, v8, v9
	v_cvt_pk_bf16_f32 v9, v10, v11
	v_cvt_pk_bf16_f32 v10, v16, v17
	v_cvt_pk_bf16_f32 v11, v12, v13
	global_store_dwordx4 v[14:15], v[8:11], off offset:256
.LBB0_1389:
	s_or_b64 exec, exec, s[16:17]
	s_nop 0
	v_add_u32_e32 v8, 0xa0, v6
	v_cmp_gt_i32_e32 vcc, s63, v8
	s_and_saveexec_b64 s[16:17], vcc
	s_cbranch_execz .LBB0_1391
	v_ashrrev_i32_e32 v9, 31, v8
	v_mad_i64_i32 v[8:9], s[4:5], s14, v239, v[8:9]
	v_lshlrev_b64 v[8:9], 12, v[8:9]
	v_lshl_add_u64 v[8:9], s[70:71], 0, v[8:9]
	v_ashrrev_i32_e32 v5, 31, v4
	v_mul_f32_e32 v2, 0x3b800000, v58
	v_pk_mul_f32 v[12:13], v[98:99], v[2:3] op_sel_hi:[1,0]
	v_pk_mul_f32 v[10:11], v[96:97], v[2:3] op_sel_hi:[1,0]
	v_pk_mul_f32 v[14:15], v[94:95], v[2:3] op_sel_hi:[1,0]
	v_pk_mul_f32 v[16:17], v[92:93], v[2:3] op_sel_hi:[1,0]
	v_cvt_pk_bf16_f32 v10, v10, v11
	v_cvt_pk_bf16_f32 v11, v12, v13
	v_cvt_pk_bf16_f32 v12, v16, v17
	v_cvt_pk_bf16_f32 v13, v14, v15
	v_lshl_add_u64 v[14:15], v[4:5], 1, v[8:9]
	global_store_dwordx4 v[14:15], v[10:13], off
	v_pk_mul_f32 v[8:9], v[88:89], v[2:3] op_sel_hi:[1,0]
	v_pk_mul_f32 v[16:17], v[84:85], v[2:3] op_sel_hi:[1,0]
	v_pk_mul_f32 v[10:11], v[90:91], v[2:3] op_sel_hi:[1,0]
	v_pk_mul_f32 v[12:13], v[86:87], v[2:3] op_sel_hi:[1,0]
	v_cvt_pk_bf16_f32 v8, v8, v9
	v_cvt_pk_bf16_f32 v9, v10, v11
	v_cvt_pk_bf16_f32 v10, v16, v17
	v_cvt_pk_bf16_f32 v11, v12, v13
	global_store_dwordx4 v[14:15], v[8:11], off offset:256
.LBB0_1391:
	s_or_b64 exec, exec, s[16:17]
	v_add_u32_e32 v6, 0xb0, v6
	v_cmp_gt_i32_e32 vcc, s63, v6
	s_and_saveexec_b64 s[16:17], vcc
	s_cbranch_execz .LBB0_1393
	v_ashrrev_i32_e32 v7, 31, v6
	v_mad_i64_i32 v[6:7], s[4:5], s14, v239, v[6:7]
	v_lshlrev_b64 v[6:7], 12, v[6:7]
	v_ashrrev_i32_e32 v5, 31, v4
	v_lshl_add_u64 v[6:7], s[70:71], 0, v[6:7]
	v_lshl_add_u64 v[12:13], v[4:5], 1, v[6:7]
	v_mul_f32_e32 v2, 0x3b800000, v59
	v_pk_mul_f32 v[6:7], v[82:83], v[2:3] op_sel_hi:[1,0]
	v_pk_mul_f32 v[4:5], v[80:81], v[2:3] op_sel_hi:[1,0]
	v_pk_mul_f32 v[8:9], v[78:79], v[2:3] op_sel_hi:[1,0]
	v_pk_mul_f32 v[10:11], v[76:77], v[2:3] op_sel_hi:[1,0]
	v_pk_mul_f32 v[14:15], v[74:75], v[2:3] op_sel_hi:[1,0]
	v_pk_mul_f32 v[16:17], v[72:73], v[2:3] op_sel_hi:[1,0]
	v_pk_mul_f32 v[18:19], v[70:71], v[2:3] op_sel_hi:[1,0]
	v_pk_mul_f32 v[20:21], v[68:69], v[2:3] op_sel_hi:[1,0]
	v_cvt_pk_bf16_f32 v4, v4, v5
	v_cvt_pk_bf16_f32 v5, v6, v7
	v_cvt_pk_bf16_f32 v6, v10, v11
	v_cvt_pk_bf16_f32 v7, v8, v9
	v_cvt_pk_bf16_f32 v8, v16, v17
	v_cvt_pk_bf16_f32 v9, v14, v15
	v_cvt_pk_bf16_f32 v10, v20, v21
	v_cvt_pk_bf16_f32 v11, v18, v19
	global_store_dwordx4 v[12:13], v[4:7], off
	global_store_dwordx4 v[12:13], v[8:11], off offset:256
